# cross-item prefetch only towards the next unit (multi-pass experts keep the plain prologue)
# speedup vs baseline: 1.0008x; 1.0008x over previous
; #define GAS __attribute__((address_space(1)))
;     ...
;     for (int vb = bid; vb < NEXP * NSLAB; vb += G) {
;         const int xcd = vb & 7, idx = vb >> 3; const int e = xcd * 8 + idx / NSLAB, slab = idx % NSLAB;
;         const int M = __builtin_amdgcn_readfirstlane(lc[LC_CNT / 4 + e]), row0 = __builtin_amdgcn_readfirstlane(lc[LC_PSTART / 4 + e]);
;         const size_t wuo = (MODE == 0) ? ((size_t)(l * NEXP + e) * D * DEXP + slab * 64) * 4 : ((size_t)(l * NEXP + e) * DEXP * D + slab * 128 + 64 * half) * 4;
;         const __amdgpu_buffer_rsrc_t wrs = __builtin_amdgcn_make_buffer_rsrc((void*)(wmat + wuo), 0, KD * LDW * 4, 0x00020000);
;         const __amdgpu_buffer_rsrc_t xrs = __builtin_amdgcn_make_buffer_rsrc((MODE == 0) ? (void*)(ws + WS_U) : (void*)((const GAS char*)(ws + WS_HID) + (size_t)row0 * LDX * 2), 0, 0x7fffffff, 0x00020000);
;         const int* el = (const int*)(ws + WS_ELIST) + (size_t)e * T;
;         for (int rp = 0; rp < M; rp += 384) {
;             unsigned xso[6];
; #pragma unroll
;             for (int i = 0; i < 6; ++i) { int tok = rp + wave * 48 + 8 * i + (lane >> 3); tok = min(tok, M - 1); if (VAR == 5) tok &= 15; if (MODE == 0) tok = el[tok]; xso[i] = (unsigned)(tok * LDX * 2 + (lane & 7) * 16); }
.LBB0_1719:
	s_add_i32 s87, s31, 0x180
	s_cmp_lt_i32 s87, s28
	s_cbranch_scc1 .Lxk_none
	s_cmp_lt_i32 s89, 1
	s_cbranch_scc1 .Lxk_none
	s_mov_b32 s84, 1
	s_add_i32 s86, s89, -1
	s_mov_b32 s87, 0
	s_add_u32 s42, s40, 0x20400
	s_addc_u32 s43, s41, 0
	s_mov_b32 s85, 0x1000000
	s_branch .Lxk_sel
.Lxk_none:
	s_mov_b32 s84, 0
	s_mov_b32 s85, 0x3a0000
	s_mov_b32 s86, 0
	s_mov_b32 s87, 0
	s_mov_b64 s[42:43], s[40:41]
	s_branch .Lxk_nel

; #define GAS __attribute__((address_space(1)))
;     ...
;     for (int vb = bid; vb < NEXP * NSLAB; vb += G) {
;         const int xcd = vb & 7, idx = vb >> 3; const int e = xcd * 8 + idx / NSLAB, slab = idx % NSLAB;
;         const int M = __builtin_amdgcn_readfirstlane(lc[LC_CNT / 4 + e]), row0 = __builtin_amdgcn_readfirstlane(lc[LC_PSTART / 4 + e]);
;         const size_t wuo = (MODE == 0) ? ((size_t)(l * NEXP + e) * D * DEXP + slab * 64) * 4 : ((size_t)(l * NEXP + e) * DEXP * D + slab * 128 + 64 * half) * 4;
;         const __amdgpu_buffer_rsrc_t wrs = __builtin_amdgcn_make_buffer_rsrc((void*)(wmat + wuo), 0, KD * LDW * 4, 0x00020000);
;         const __amdgpu_buffer_rsrc_t xrs = __builtin_amdgcn_make_buffer_rsrc((MODE == 0) ? (void*)(ws + WS_U) : (void*)((const GAS char*)(ws + WS_HID) + (size_t)row0 * LDX * 2), 0, 0x7fffffff, 0x00020000);
;         const int* el = (const int*)(ws + WS_ELIST) + (size_t)e * T;
;         for (int rp = 0; rp < M; rp += 384) {
;             unsigned xso[6];
; #pragma unroll
;             for (int i = 0; i < 6; ++i) { int tok = rp + wave * 48 + 8 * i + (lane >> 3); tok = min(tok, M - 1); if (VAR == 5) tok &= 15; if (MODE == 0) tok = el[tok]; xso[i] = (unsigned)(tok * LDX * 2 + (lane & 7) * 16); }
.LBB0_1784:
	s_add_i32 s87, s31, 0x180
	s_cmp_lt_i32 s87, s30
	s_cbranch_scc1 .Lxl_none
	s_cmp_lt_i32 s89, 1
	s_cbranch_scc1 .Lxl_none
	s_mov_b32 s84, 1
	s_add_i32 s86, s89, -1
	s_mov_b32 s87, 0
	s_sub_i32 s88, s90, s24
	s_mov_b32 s85, 0x800000
	s_branch .Lxl_sel
.Lxl_none:
	s_mov_b32 s84, 0
	s_mov_b32 s85, 0x280000
	s_mov_b32 s86, 0
	s_mov_b32 s87, 0
	s_mov_b32 s88, 0

.LBB0_1785:
	s_add_i32 s2, s2, 2
	s_min_u32 s3, s2, 4
	s_lshl_b32 s33, s3, 19
	s_add_i32 s33, s33, 0x180000
	s_add_i32 s40, s85, 0x80000
	s_cmp_gt_u32 s2, 4
	s_cselect_b32 s33, s40, s33
	s_waitcnt vmcnt(10)
	v_cvt_pk_bf16_f32 v164, v2, v10
	s_waitcnt vmcnt(7)
	v_cvt_pk_bf16_f32 v165, v6, v14
	v_cvt_pk_bf16_f32 v166, v3, v11
	v_cvt_pk_bf16_f32 v167, v7, v15
	v_cvt_pk_bf16_f32 v190, v4, v12
	v_cvt_pk_bf16_f32 v191, v8, v16
	v_cvt_pk_bf16_f32 v192, v5, v13
	v_cvt_pk_bf16_f32 v193, v9, v17
	buffer_load_dwordx4 v[2:5], v160, s[8:11], s33 offen nt
	buffer_load_dwordx4 v[10:13], v90, s[8:11], s33 offen nt
	buffer_load_dwordx4 v[6:9], v178, s[8:11], s33 offen nt
	buffer_load_dwordx4 v[14:17], v179, s[8:11], s33 offen nt
	v_add_u32_e32 v194, 0x4000, v188
	v_add_u32_e32 v195, 0x4000, v180
	v_add_u32_e32 v214, v173, v174
	ds_write2_b64 v194, v[164:165], v[166:167] offset1:16
	ds_write2_b64 v195, v[190:191], v[192:193] offset0:32 offset1:48
	v_add_u32_e32 v215, v176, v174
	ds_read_b128 v[164:167], v214 offset:32768
	ds_read_b128 v[190:193], v214 offset:34816
	ds_read_b128 v[194:197], v214 offset:36864
	ds_read_b128 v[198:201], v215
	ds_read_b128 v[202:205], v215 offset:2048
	ds_read_b128 v[206:209], v215 offset:4096
	ds_read_b128 v[210:213], v215 offset:6144
	s_waitcnt lgkmcnt(3)
	v_mfma_f32_16x16x32_bf16 v[152:155], v[198:201], v[164:167], v[152:155]
	v_mfma_f32_16x16x32_bf16 v[120:123], v[198:201], v[190:193], v[120:123]
	v_mfma_f32_16x16x32_bf16 v[62:65], v[198:201], v[194:197], v[62:65]
	s_waitcnt lgkmcnt(2)
	v_mfma_f32_16x16x32_bf16 v[148:151], v[202:205], v[164:167], v[148:151]
	v_mfma_f32_16x16x32_bf16 v[96:99], v[202:205], v[190:193], v[96:99]
	v_mfma_f32_16x16x32_bf16 v[58:61], v[202:205], v[194:197], v[58:61]
	s_waitcnt lgkmcnt(1)
	v_mfma_f32_16x16x32_bf16 v[144:147], v[206:209], v[164:167], v[144:147]
	v_mfma_f32_16x16x32_bf16 v[86:89], v[206:209], v[190:193], v[86:89]
	v_mfma_f32_16x16x32_bf16 v[54:57], v[206:209], v[194:197], v[54:57]
	s_waitcnt lgkmcnt(0)
	v_mfma_f32_16x16x32_bf16 v[140:143], v[210:213], v[164:167], v[140:143]
	v_mfma_f32_16x16x32_bf16 v[82:85], v[210:213], v[190:193], v[82:85]
	v_mfma_f32_16x16x32_bf16 v[50:53], v[210:213], v[194:197], v[50:53]
	ds_read_b128 v[198:201], v215 offset:8192
	ds_read_b128 v[202:205], v215 offset:10240
	ds_read_b128 v[206:209], v215 offset:12288
	ds_read_b128 v[210:213], v215 offset:14336
	s_waitcnt lgkmcnt(3)
	v_mfma_f32_16x16x32_bf16 v[136:139], v[198:201], v[164:167], v[136:139]
	v_mfma_f32_16x16x32_bf16 v[78:81], v[198:201], v[190:193], v[78:81]
	v_mfma_f32_16x16x32_bf16 v[46:49], v[198:201], v[194:197], v[46:49]
	s_waitcnt lgkmcnt(2)
	v_mfma_f32_16x16x32_bf16 v[132:135], v[202:205], v[164:167], v[132:135]
	v_mfma_f32_16x16x32_bf16 v[74:77], v[202:205], v[190:193], v[74:77]
	v_mfma_f32_16x16x32_bf16 v[42:45], v[202:205], v[194:197], v[42:45]
	s_waitcnt lgkmcnt(1)
	v_mfma_f32_16x16x32_bf16 v[128:131], v[206:209], v[164:167], v[128:131]
	v_mfma_f32_16x16x32_bf16 v[70:73], v[206:209], v[190:193], v[70:73]
	v_mfma_f32_16x16x32_bf16 v[38:41], v[206:209], v[194:197], v[38:41]
	s_waitcnt lgkmcnt(0)
	v_mfma_f32_16x16x32_bf16 v[124:127], v[210:213], v[164:167], v[124:127]
	v_mfma_f32_16x16x32_bf16 v[66:69], v[210:213], v[190:193], v[66:69]
	v_mfma_f32_16x16x32_bf16 v[34:37], v[210:213], v[194:197], v[34:37]
	v_add_u32_e32 v216, v173, v175
	ds_read_b128 v[164:167], v216 offset:32768
	ds_read_b128 v[190:193], v216 offset:34816
	v_add_u32_e32 v217, v176, v175
	ds_read_b128 v[194:197], v216 offset:36864
	ds_read_b128 v[198:201], v217
	ds_read_b128 v[202:205], v217 offset:2048
	ds_read_b128 v[206:209], v217 offset:4096
	ds_read_b128 v[210:213], v217 offset:6144
	s_waitcnt lgkmcnt(3)
	v_mfma_f32_16x16x32_bf16 v[152:155], v[198:201], v[164:167], v[152:155]
	v_mfma_f32_16x16x32_bf16 v[120:123], v[198:201], v[190:193], v[120:123]
	v_mfma_f32_16x16x32_bf16 v[62:65], v[198:201], v[194:197], v[62:65]
	s_waitcnt lgkmcnt(2)
	v_mfma_f32_16x16x32_bf16 v[148:151], v[202:205], v[164:167], v[148:151]
	v_mfma_f32_16x16x32_bf16 v[96:99], v[202:205], v[190:193], v[96:99]
	v_mfma_f32_16x16x32_bf16 v[58:61], v[202:205], v[194:197], v[58:61]
	s_waitcnt lgkmcnt(1)
	v_mfma_f32_16x16x32_bf16 v[144:147], v[206:209], v[164:167], v[144:147]
	v_mfma_f32_16x16x32_bf16 v[86:89], v[206:209], v[190:193], v[86:89]
	v_mfma_f32_16x16x32_bf16 v[54:57], v[206:209], v[194:197], v[54:57]
	s_waitcnt lgkmcnt(0)
	v_mfma_f32_16x16x32_bf16 v[140:143], v[210:213], v[164:167], v[140:143]
	v_mfma_f32_16x16x32_bf16 v[82:85], v[210:213], v[190:193], v[82:85]
	v_mfma_f32_16x16x32_bf16 v[50:53], v[210:213], v[194:197], v[50:53]
	ds_read_b128 v[198:201], v217 offset:8192
	ds_read_b128 v[202:205], v217 offset:10240
	ds_read_b128 v[206:209], v217 offset:12288
	ds_read_b128 v[210:213], v217 offset:14336
	s_min_u32 s33, s2, 5
	s_lshl_b32 s33, s33, 7
	s_waitcnt vmcnt(9)
	ds_write_b128 v189, v[104:107] offset:38912
	s_waitcnt vmcnt(8)
	ds_write_b128 v181, v[92:95] offset:39936
	s_waitcnt vmcnt(7)
	ds_write_b128 v189, v[112:115] offset:40960
	s_waitcnt vmcnt(6)
	ds_write_b128 v181, v[116:119] offset:41984
	s_waitcnt vmcnt(5)
	ds_write_b128 v189, v[100:103] offset:43008
	s_waitcnt vmcnt(4)
	ds_write_b128 v181, v[108:111] offset:44032
	s_addk_i32 s33, 0x100
	s_cmp_lt_u32 s2, 6
	s_cbranch_scc1 .Lxl_nx0
	s_cmp_eq_u32 s84, 0
	s_cbranch_scc1 .Lxl_nx0
	s_mov_b32 s33, 0
	v_add_u32_e32 v252, s87, v162
	v_min_i32_e32 v253, s86, v252
	v_add_u32_e32 v253, s88, v253
	v_lshl_or_b32 v182, v253, 10, v163
	v_or_b32_e32 v253, 8, v252
	v_min_i32_e32 v253, s86, v253
	v_add_u32_e32 v253, s88, v253
	v_lshl_or_b32 v183, v253, 10, v163
	v_add_u32_e32 v253, 0x80, v252
	v_min_i32_e32 v253, s86, v253
	v_add_u32_e32 v253, s88, v253
	v_lshl_or_b32 v184, v253, 10, v163
	v_add_u32_e32 v253, 0x88, v252
	v_min_i32_e32 v253, s86, v253
	v_add_u32_e32 v253, s88, v253
	v_lshl_or_b32 v185, v253, 10, v163
	v_add_u32_e32 v253, 0x100, v252
	v_min_i32_e32 v253, s86, v253
	v_add_u32_e32 v253, s88, v253
	v_lshl_or_b32 v186, v253, 10, v163
	v_add_u32_e32 v253, 0x108, v252
	v_min_i32_e32 v253, s86, v253
	v_add_u32_e32 v253, s88, v253
	v_lshl_or_b32 v187, v253, 10, v163

.Lmoe_l_b:
	s_add_i32 s2, s2, 2
	s_min_u32 s3, s2, 4
	s_lshl_b32 s33, s3, 19
	s_add_i32 s33, s33, 0x180000
	s_add_i32 s40, s85, 0x80000
	s_cmp_gt_u32 s2, 4
	s_cselect_b32 s33, s40, s33
	s_waitcnt vmcnt(10)
	v_cvt_pk_bf16_f32 v164, v2, v10
	s_waitcnt vmcnt(7)
	v_cvt_pk_bf16_f32 v165, v6, v14
	v_cvt_pk_bf16_f32 v166, v3, v11
	v_cvt_pk_bf16_f32 v167, v7, v15
	v_cvt_pk_bf16_f32 v190, v4, v12
	v_cvt_pk_bf16_f32 v191, v8, v16
	v_cvt_pk_bf16_f32 v192, v5, v13
	v_cvt_pk_bf16_f32 v193, v9, v17
	buffer_load_dwordx4 v[2:5], v160, s[8:11], s33 offen nt
	buffer_load_dwordx4 v[10:13], v90, s[8:11], s33 offen nt
	buffer_load_dwordx4 v[6:9], v178, s[8:11], s33 offen nt
	buffer_load_dwordx4 v[14:17], v179, s[8:11], s33 offen nt
	v_add_u32_e32 v194, 0x4000, v188
	v_add_u32_e32 v195, 0x4000, v180
	v_add_u32_e32 v214, v173, v174
	ds_write2_b64 v194, v[164:165], v[166:167] offset1:16
	ds_write2_b64 v195, v[190:191], v[192:193] offset0:32 offset1:48
	v_add_u32_e32 v215, v176, v174
	ds_read_b128 v[164:167], v214 offset:32768
	ds_read_b128 v[190:193], v214 offset:34816
	ds_read_b128 v[198:201], v215
	ds_read_b128 v[202:205], v215 offset:2048
	ds_read_b128 v[206:209], v215 offset:4096
	ds_read_b128 v[210:213], v215 offset:6144
	s_waitcnt lgkmcnt(3)
	v_mfma_f32_16x16x32_bf16 v[152:155], v[198:201], v[164:167], v[152:155]
	v_mfma_f32_16x16x32_bf16 v[120:123], v[198:201], v[190:193], v[120:123]
	s_waitcnt lgkmcnt(2)
	v_mfma_f32_16x16x32_bf16 v[148:151], v[202:205], v[164:167], v[148:151]
	v_mfma_f32_16x16x32_bf16 v[96:99], v[202:205], v[190:193], v[96:99]
	s_waitcnt lgkmcnt(1)
	v_mfma_f32_16x16x32_bf16 v[144:147], v[206:209], v[164:167], v[144:147]
	v_mfma_f32_16x16x32_bf16 v[86:89], v[206:209], v[190:193], v[86:89]
	s_waitcnt lgkmcnt(0)
	v_mfma_f32_16x16x32_bf16 v[140:143], v[210:213], v[164:167], v[140:143]
	v_mfma_f32_16x16x32_bf16 v[82:85], v[210:213], v[190:193], v[82:85]
	ds_read_b128 v[198:201], v215 offset:8192
	ds_read_b128 v[202:205], v215 offset:10240
	ds_read_b128 v[206:209], v215 offset:12288
	ds_read_b128 v[210:213], v215 offset:14336
	s_waitcnt lgkmcnt(3)
	v_mfma_f32_16x16x32_bf16 v[136:139], v[198:201], v[164:167], v[136:139]
	v_mfma_f32_16x16x32_bf16 v[78:81], v[198:201], v[190:193], v[78:81]
	s_waitcnt lgkmcnt(2)
	v_mfma_f32_16x16x32_bf16 v[132:135], v[202:205], v[164:167], v[132:135]
	v_mfma_f32_16x16x32_bf16 v[74:77], v[202:205], v[190:193], v[74:77]
	s_waitcnt lgkmcnt(1)
	v_mfma_f32_16x16x32_bf16 v[128:131], v[206:209], v[164:167], v[128:131]
	v_mfma_f32_16x16x32_bf16 v[70:73], v[206:209], v[190:193], v[70:73]
	s_waitcnt lgkmcnt(0)
	v_mfma_f32_16x16x32_bf16 v[124:127], v[210:213], v[164:167], v[124:127]
	v_mfma_f32_16x16x32_bf16 v[66:69], v[210:213], v[190:193], v[66:69]
	v_add_u32_e32 v216, v173, v175
	ds_read_b128 v[164:167], v216 offset:32768
	ds_read_b128 v[190:193], v216 offset:34816
	v_add_u32_e32 v217, v176, v175
	ds_read_b128 v[198:201], v217
	ds_read_b128 v[202:205], v217 offset:2048
	ds_read_b128 v[206:209], v217 offset:4096
	ds_read_b128 v[210:213], v217 offset:6144
	s_waitcnt lgkmcnt(3)
	v_mfma_f32_16x16x32_bf16 v[152:155], v[198:201], v[164:167], v[152:155]
	v_mfma_f32_16x16x32_bf16 v[120:123], v[198:201], v[190:193], v[120:123]
	s_waitcnt lgkmcnt(2)
	v_mfma_f32_16x16x32_bf16 v[148:151], v[202:205], v[164:167], v[148:151]
	v_mfma_f32_16x16x32_bf16 v[96:99], v[202:205], v[190:193], v[96:99]
	s_waitcnt lgkmcnt(1)
	v_mfma_f32_16x16x32_bf16 v[144:147], v[206:209], v[164:167], v[144:147]
	v_mfma_f32_16x16x32_bf16 v[86:89], v[206:209], v[190:193], v[86:89]
	s_waitcnt lgkmcnt(0)
	v_mfma_f32_16x16x32_bf16 v[140:143], v[210:213], v[164:167], v[140:143]
	v_mfma_f32_16x16x32_bf16 v[82:85], v[210:213], v[190:193], v[82:85]
	ds_read_b128 v[198:201], v217 offset:8192
	ds_read_b128 v[202:205], v217 offset:10240
	ds_read_b128 v[206:209], v217 offset:12288
	ds_read_b128 v[210:213], v217 offset:14336
	s_min_u32 s33, s2, 5
	s_lshl_b32 s33, s33, 7
	s_waitcnt vmcnt(7)
	ds_write_b128 v189, v[104:107] offset:38912
	s_waitcnt vmcnt(6)
	ds_write_b128 v181, v[92:95] offset:39936
	s_waitcnt vmcnt(5)
	ds_write_b128 v189, v[112:115] offset:40960
	s_waitcnt vmcnt(4)
	ds_write_b128 v181, v[116:119] offset:41984
	s_addk_i32 s33, 0x100
	s_cmp_lt_u32 s2, 6
	s_cbranch_scc1 .Lxl_nx1
	s_cmp_eq_u32 s84, 0
	s_cbranch_scc1 .Lxl_nx1
	s_mov_b32 s33, 0
	v_add_u32_e32 v252, s87, v162
	v_min_i32_e32 v253, s86, v252
	v_add_u32_e32 v253, s88, v253
	v_lshl_or_b32 v182, v253, 10, v163
	v_or_b32_e32 v253, 8, v252
	v_min_i32_e32 v253, s86, v253
	v_add_u32_e32 v253, s88, v253
	v_lshl_or_b32 v183, v253, 10, v163
	v_add_u32_e32 v253, 0x80, v252
	v_min_i32_e32 v253, s86, v253
	v_add_u32_e32 v253, s88, v253
	v_lshl_or_b32 v184, v253, 10, v163
	v_add_u32_e32 v253, 0x88, v252
	v_min_i32_e32 v253, s86, v253
	v_add_u32_e32 v253, s88, v253
	v_lshl_or_b32 v185, v253, 10, v163
	v_add_u32_e32 v253, 0x100, v252
	v_min_i32_e32 v253, s86, v253
	v_add_u32_e32 v253, s88, v253
	v_lshl_or_b32 v186, v253, 10, v163
	v_add_u32_e32 v253, 0x108, v252
	v_min_i32_e32 v253, s86, v253
	v_add_u32_e32 v253, s88, v253
	v_lshl_or_b32 v187, v253, 10, v163
